# combo8 + strategy 1 (counted waits): P0 weight-transpose loops no longer wait for the previous tile's two store acks before the LDS writes (vmcnt 9..2, two dummy loads shape the first iteration)
# speedup vs baseline: 1.0060x; 1.0060x over previous
.LBB0_29:
	s_mov_b32 s1, 0
	s_mov_b32 s2, 0
	s_cmpk_gt_i32 s68, 0xbff
	s_cbranch_scc1 .LBB0_36
	v_mbcnt_lo_u32_b32 v0, -1, s2
	v_mbcnt_hi_u32_b32 v40, -1, v0
	v_readlane_b32 s2, v254, 4
	s_add_u32 s4, s48, 0x8400000
	v_readlane_b32 s3, v254, 5
	v_add_u32_e32 v37, s2, v40
	s_mul_hi_i32 s2, s68, 0x2aaaaaab
	s_addc_u32 s5, s49, 0
	s_lshr_b32 s3, s2, 31
	s_ashr_i32 s2, s2, 5
	s_add_i32 s2, s2, s3
	s_mul_i32 s3, s2, 0xc0
	s_sub_i32 s3, s68, s3
	v_ashrrev_i32_e32 v36, 4, v37
	v_lshl_add_u32 v30, s2, 8, v36
	s_lshl_b32 s2, s3, 6
	s_ashr_i32 s3, s2, 31
	s_lshl_b64 s[2:3], s[2:3], 2
	s_add_u32 s2, s24, s2
	v_lshlrev_b32_e32 v0, 4, v40
	s_addc_u32 s3, s25, s3
	v_and_b32_e32 v32, 0xf0, v0
	v_mov_b32_e32 v33, 0
	v_lshl_add_u64 v[24:25], s[2:3], 0, v[32:33]
	s_mov_b32 s2, 0xc040
	v_mad_i64_i32 v[8:9], s[6:7], v30, s2, v[24:25]
	v_add_u32_e32 v0, 32, v30
	v_mad_i64_i32 v[10:11], s[6:7], v0, s2, v[24:25]
	global_load_dwordx4 v[0:3], v[8:9], off
	global_load_dwordx4 v[4:7], v[10:11], off
	v_add_u32_e32 v8, 64, v30
	v_mad_i64_i32 v[16:17], s[6:7], v8, s2, v[24:25]
	v_add_u32_e32 v8, 0x60, v30
	v_mad_i64_i32 v[18:19], s[6:7], v8, s2, v[24:25]
	global_load_dwordx4 v[8:11], v[16:17], off
	global_load_dwordx4 v[12:15], v[18:19], off
	v_add_u32_e32 v16, 0x80, v30
	v_mad_i64_i32 v[26:27], s[6:7], v16, s2, v[24:25]
	v_add_u32_e32 v16, 0xa0, v30
	v_mad_i64_i32 v[28:29], s[6:7], v16, s2, v[24:25]
	global_load_dwordx4 v[16:19], v[26:27], off
	global_load_dwordx4 v[20:23], v[28:29], off
	v_add_u32_e32 v26, 0xc0, v30
	v_mad_i64_i32 v[34:35], s[6:7], v26, s2, v[24:25]
	v_add_u32_e32 v26, 0xe0, v30
	v_mad_i64_i32 v[38:39], s[6:7], v26, s2, v[24:25]
	global_load_dwordx4 v[24:27], v[34:35], off
	global_load_dwordx4 v[28:31], v[38:39], off
	v_add_u32_e32 v39, 0, v32
	v_lshl_add_u64 v[34:35], s[24:25], 0, v[32:33]
	v_lshlrev_b32_e32 v32, 5, v40
	v_ashrrev_i32_e32 v37, 3, v37
	v_and_b32_e32 v32, 0xe0, v32
	s_movk_i32 s3, 0x104
	v_mul_u32_u24_e32 v38, 0x104, v32
	v_lshlrev_b32_e32 v40, 2, v37
	v_add3_u32 v38, 0, v38, v40
	v_mul_lo_u32 v40, v36, s3
	v_add_u32_e32 v39, v39, v40
	s_lshl_b32 s10, s68, 6
	s_lshl_b32 s3, s46, 6
	v_add_u32_e32 v40, 0x2080, v39
	v_add_u32_e32 v41, 0x2088, v39
	v_add_u32_e32 v42, 0x4100, v39
	v_add_u32_e32 v43, 0x4108, v39
	v_add_u32_e32 v44, 0x6180, v39
	v_add_u32_e32 v45, 0x6188, v39
	v_add_u32_e32 v46, 0x8200, v39
	v_add_u32_e32 v47, 0x8208, v39
	v_add_u32_e32 v48, 0xa280, v39
	v_add_u32_e32 v49, 0xa288, v39
	v_add_u32_e32 v50, 0xc300, v39
	v_add_u32_e32 v51, 0xc308, v39
	v_add_u32_e32 v52, 0xe380, v39
	s_mov_b32 s31, s68
	global_load_dword v200, v[34:35], off
	global_load_dword v200, v[34:35], off
	s_branch .LBB0_32

.LBB0_32:
	s_add_i32 s11, s31, s46
	s_cmpk_gt_i32 s11, 0xbff
	v_add_u32_e32 v53, 0xe388, v39
	s_cselect_b64 s[6:7], -1, 0
	s_cmpk_lt_i32 s11, 0xc00
	s_mov_b64 s[8:9], -1
	s_waitcnt vmcnt(9)
	ds_write2_b32 v39, v0, v1 offset1:1
	ds_write2_b32 v39, v2, v3 offset0:2 offset1:3
	s_waitcnt vmcnt(8)
	ds_write2_b32 v40, v4, v5 offset1:1
	ds_write2_b32 v41, v6, v7 offset1:1
	s_waitcnt vmcnt(7)
	ds_write2_b32 v42, v8, v9 offset1:1
	ds_write2_b32 v43, v10, v11 offset1:1
	s_waitcnt vmcnt(6)
	ds_write2_b32 v44, v12, v13 offset1:1
	ds_write2_b32 v45, v14, v15 offset1:1
	s_waitcnt vmcnt(5)
	ds_write2_b32 v46, v16, v17 offset1:1
	ds_write2_b32 v47, v18, v19 offset1:1
	s_waitcnt vmcnt(4)
	ds_write2_b32 v48, v20, v21 offset1:1
	ds_write2_b32 v49, v22, v23 offset1:1
	s_waitcnt vmcnt(3)
	ds_write2_b32 v50, v24, v25 offset1:1
	ds_write2_b32 v51, v26, v27 offset1:1
	s_waitcnt vmcnt(2)
	ds_write2_b32 v52, v28, v29 offset1:1
	ds_write2_b32 v53, v30, v31 offset1:1
	s_waitcnt lgkmcnt(0)
	s_barrier
	s_cbranch_scc1 .LBB0_34
	s_add_i32 s30, s10, s3
	s_mov_b64 s[8:9], 0

.LBB0_36:
	s_cmpk_lt_i32 s68, 0x400
	s_cselect_b64 s[4:5], -1, 0
	s_cmpk_gt_i32 s68, 0x3ff
	s_cbranch_scc1 .LBB0_43
	s_add_u32 s6, s48, 0xe400000
	s_addc_u32 s7, s49, 0
	s_waitcnt vmcnt(9)
	v_mbcnt_lo_u32_b32 v0, -1, s1
	s_ashr_i32 s1, s68, 31
	s_lshr_b32 s1, s1, 26
	v_mbcnt_hi_u32_b32 v40, -1, v0
	v_readlane_b32 s2, v254, 4
	s_add_i32 s1, s68, s1
	v_readlane_b32 s3, v254, 5
	v_add_u32_e32 v37, s2, v40
	s_and_b32 s2, s1, 0x3ffffc0
	s_sub_i32 s2, s68, s2
	s_lshl_b32 s2, s2, 6
	s_lshl_b32 s1, s1, 2
	s_ashr_i32 s3, s2, 31
	v_ashrrev_i32_e32 v36, 4, v37
	s_and_b32 s1, s1, 0xffffff00
	s_lshl_b64 s[2:3], s[2:3], 2
	s_waitcnt vmcnt(3)
	v_add_u32_e32 v24, s1, v36
	s_add_u32 s2, s28, s2
	v_lshlrev_b32_e32 v0, 4, v40
	s_addc_u32 s3, s29, s3
	v_and_b32_e32 v32, 0xf0, v0
	v_mov_b32_e32 v33, 0
	v_ashrrev_i32_e32 v25, 31, v24
	v_lshl_add_u64 v[26:27], s[2:3], 0, v[32:33]
	v_lshlrev_b64 v[0:1], 14, v[24:25]
	v_lshl_add_u64 v[8:9], v[26:27], 0, v[0:1]
	v_add_u32_e32 v0, 32, v24
	v_ashrrev_i32_e32 v1, 31, v0
	v_lshlrev_b64 v[0:1], 14, v[0:1]
	v_lshl_add_u64 v[10:11], v[26:27], 0, v[0:1]
	global_load_dwordx4 v[0:3], v[8:9], off
	global_load_dwordx4 v[4:7], v[10:11], off
	v_add_u32_e32 v8, 64, v24
	v_ashrrev_i32_e32 v9, 31, v8
	v_lshlrev_b64 v[8:9], 14, v[8:9]
	v_lshl_add_u64 v[16:17], v[26:27], 0, v[8:9]
	v_add_u32_e32 v8, 0x60, v24
	v_ashrrev_i32_e32 v9, 31, v8
	v_lshlrev_b64 v[8:9], 14, v[8:9]
	v_lshl_add_u64 v[18:19], v[26:27], 0, v[8:9]
	global_load_dwordx4 v[8:11], v[16:17], off
	global_load_dwordx4 v[12:15], v[18:19], off
	v_add_u32_e32 v16, 0x80, v24
	v_ashrrev_i32_e32 v17, 31, v16
	v_lshlrev_b64 v[16:17], 14, v[16:17]
	s_waitcnt vmcnt(6)
	v_lshl_add_u64 v[28:29], v[26:27], 0, v[16:17]
	v_add_u32_e32 v16, 0xa0, v24
	v_ashrrev_i32_e32 v17, 31, v16
	v_lshlrev_b64 v[16:17], 14, v[16:17]
	v_lshl_add_u64 v[30:31], v[26:27], 0, v[16:17]
	global_load_dwordx4 v[16:19], v[28:29], off
	global_load_dwordx4 v[20:23], v[30:31], off
	v_add_u32_e32 v28, 0xc0, v24
	v_ashrrev_i32_e32 v29, 31, v28
	v_add_u32_e32 v24, 0xe0, v24
	v_lshlrev_b64 v[28:29], 14, v[28:29]
	v_ashrrev_i32_e32 v25, 31, v24
	v_lshl_add_u64 v[34:35], v[26:27], 0, v[28:29]
	v_lshlrev_b64 v[24:25], 14, v[24:25]
	v_lshl_add_u64 v[38:39], v[26:27], 0, v[24:25]
	global_load_dwordx4 v[24:27], v[34:35], off
	global_load_dwordx4 v[28:31], v[38:39], off
	v_add_u32_e32 v39, 0, v32
	v_lshl_add_u64 v[34:35], s[28:29], 0, v[32:33]
	v_lshlrev_b32_e32 v32, 5, v40
	v_ashrrev_i32_e32 v37, 3, v37
	v_and_b32_e32 v32, 0xe0, v32
	s_movk_i32 s1, 0x104
	v_mul_u32_u24_e32 v38, 0x104, v32
	v_lshlrev_b32_e32 v40, 2, v37
	v_add3_u32 v38, 0, v38, v40
	v_mul_lo_u32 v40, v36, s1
	s_lshl_b32 s2, s68, 6
	s_lshl_b32 s1, s46, 6
	v_add_u32_e32 v39, v39, v40
	s_mov_b32 s29, s68
	global_load_dword v200, v[34:35], off
	global_load_dword v200, v[34:35], off
	s_branch .LBB0_39

.LBB0_39:
	v_add_u32_e32 v40, 0x2080, v39
	s_waitcnt vmcnt(9)
	ds_write2_b32 v39, v0, v1 offset1:1
	ds_write2_b32 v39, v2, v3 offset0:2 offset1:3
	s_waitcnt vmcnt(8)
	ds_write2_b32 v40, v4, v5 offset1:1
	v_add_u32_e32 v40, 0x2088, v39
	ds_write2_b32 v40, v6, v7 offset1:1
	v_add_u32_e32 v40, 0x4100, v39
	s_waitcnt vmcnt(7)
	ds_write2_b32 v40, v8, v9 offset1:1
	v_add_u32_e32 v40, 0x4108, v39
	ds_write2_b32 v40, v10, v11 offset1:1
	v_add_u32_e32 v40, 0x6180, v39
	s_waitcnt vmcnt(6)
	ds_write2_b32 v40, v12, v13 offset1:1
	v_add_u32_e32 v40, 0x6188, v39
	ds_write2_b32 v40, v14, v15 offset1:1
	v_add_u32_e32 v40, 0x8200, v39
	s_waitcnt vmcnt(5)
	ds_write2_b32 v40, v16, v17 offset1:1
	v_add_u32_e32 v40, 0x8208, v39
	ds_write2_b32 v40, v18, v19 offset1:1
	v_add_u32_e32 v40, 0xa280, v39
	s_waitcnt vmcnt(4)
	ds_write2_b32 v40, v20, v21 offset1:1
	v_add_u32_e32 v40, 0xa288, v39
	ds_write2_b32 v40, v22, v23 offset1:1
	v_add_u32_e32 v40, 0xc300, v39
	s_waitcnt vmcnt(3)
	ds_write2_b32 v40, v24, v25 offset1:1
	v_add_u32_e32 v40, 0xc308, v39
	s_add_i32 s3, s29, s46
	ds_write2_b32 v40, v26, v27 offset1:1
	v_add_u32_e32 v40, 0xe380, v39
	s_cmpk_gt_i32 s3, 0x3ff
	s_waitcnt vmcnt(2)
	ds_write2_b32 v40, v28, v29 offset1:1
	v_add_u32_e32 v40, 0xe388, v39
	s_cselect_b64 s[8:9], -1, 0
	s_cmpk_lt_i32 s3, 0x400
	s_mov_b64 s[10:11], -1
	ds_write2_b32 v40, v30, v31 offset1:1
	s_waitcnt lgkmcnt(0)
	s_barrier
	s_cbranch_scc1 .LBB0_41
	s_add_i32 s28, s2, s1
	s_mov_b64 s[10:11], 0

.LBB0_43:
	s_mov_b32 s1, 0
	s_mov_b32 s2, 0
	s_cmpk_gt_i32 s68, 0xfff
	s_cbranch_scc1 .LBB0_50
	s_waitcnt vmcnt(9)
	v_mbcnt_lo_u32_b32 v0, -1, s2
	s_add_u32 s6, s48, 0x19400000
	v_mbcnt_hi_u32_b32 v40, -1, v0
	v_readlane_b32 s2, v254, 4
	s_addc_u32 s7, s49, 0
	v_readlane_b32 s3, v254, 5
	v_add_u32_e32 v37, s2, v40
	s_ashr_i32 s2, s68, 31
	s_lshr_b32 s2, s2, 26
	s_add_i32 s2, s68, s2
	s_and_b32 s3, s2, 0x3ffffc0
	s_lshl_b32 s2, s2, 2
	s_sub_i32 s3, s68, s3
	v_ashrrev_i32_e32 v36, 4, v37
	s_and_b32 s2, s2, 0xffffff00
	s_waitcnt vmcnt(3)
	v_add_u32_e32 v24, s2, v36
	s_lshl_b32 s2, s3, 6
	s_ashr_i32 s3, s2, 31
	s_lshl_b64 s[2:3], s[2:3], 2
	s_add_u32 s2, s26, s2
	v_lshlrev_b32_e32 v0, 4, v40
	s_addc_u32 s3, s27, s3
	v_and_b32_e32 v32, 0xf0, v0
	v_mov_b32_e32 v33, 0
	v_ashrrev_i32_e32 v25, 31, v24
	v_lshl_add_u64 v[26:27], s[2:3], 0, v[32:33]
	v_lshlrev_b64 v[0:1], 14, v[24:25]
	v_lshl_add_u64 v[8:9], v[26:27], 0, v[0:1]
	v_add_u32_e32 v0, 32, v24
	v_ashrrev_i32_e32 v1, 31, v0
	v_lshlrev_b64 v[0:1], 14, v[0:1]
	v_lshl_add_u64 v[10:11], v[26:27], 0, v[0:1]
	global_load_dwordx4 v[0:3], v[8:9], off
	global_load_dwordx4 v[4:7], v[10:11], off
	v_add_u32_e32 v8, 64, v24
	v_ashrrev_i32_e32 v9, 31, v8
	v_lshlrev_b64 v[8:9], 14, v[8:9]
	v_lshl_add_u64 v[16:17], v[26:27], 0, v[8:9]
	v_add_u32_e32 v8, 0x60, v24
	v_ashrrev_i32_e32 v9, 31, v8
	v_lshlrev_b64 v[8:9], 14, v[8:9]
	v_lshl_add_u64 v[18:19], v[26:27], 0, v[8:9]
	global_load_dwordx4 v[8:11], v[16:17], off
	global_load_dwordx4 v[12:15], v[18:19], off
	v_add_u32_e32 v16, 0x80, v24
	v_ashrrev_i32_e32 v17, 31, v16
	v_lshlrev_b64 v[16:17], 14, v[16:17]
	s_waitcnt vmcnt(6)
	v_lshl_add_u64 v[28:29], v[26:27], 0, v[16:17]
	v_add_u32_e32 v16, 0xa0, v24
	v_ashrrev_i32_e32 v17, 31, v16
	v_lshlrev_b64 v[16:17], 14, v[16:17]
	v_lshl_add_u64 v[30:31], v[26:27], 0, v[16:17]
	global_load_dwordx4 v[16:19], v[28:29], off
	global_load_dwordx4 v[20:23], v[30:31], off
	v_add_u32_e32 v28, 0xc0, v24
	v_ashrrev_i32_e32 v29, 31, v28
	v_add_u32_e32 v24, 0xe0, v24
	v_lshlrev_b64 v[28:29], 14, v[28:29]
	v_ashrrev_i32_e32 v25, 31, v24
	v_lshl_add_u64 v[34:35], v[26:27], 0, v[28:29]
	v_lshlrev_b64 v[24:25], 14, v[24:25]
	v_lshl_add_u64 v[38:39], v[26:27], 0, v[24:25]
	global_load_dwordx4 v[24:27], v[34:35], off
	global_load_dwordx4 v[28:31], v[38:39], off
	v_add_u32_e32 v39, 0, v32
	v_lshl_add_u64 v[34:35], s[26:27], 0, v[32:33]
	v_lshlrev_b32_e32 v32, 5, v40
	v_ashrrev_i32_e32 v37, 3, v37
	v_and_b32_e32 v32, 0xe0, v32
	s_movk_i32 s2, 0x104
	v_mul_u32_u24_e32 v38, 0x104, v32
	v_lshlrev_b32_e32 v40, 2, v37
	v_add3_u32 v38, 0, v38, v40
	v_mul_lo_u32 v40, v36, s2
	s_lshl_b32 s3, s68, 6
	s_lshl_b32 s2, s46, 6
	v_add_u32_e32 v39, v39, v40
	s_mov_b32 s28, s68
	global_load_dword v200, v[34:35], off
	global_load_dword v200, v[34:35], off
	s_branch .LBB0_46

.LBB0_46:
	v_add_u32_e32 v40, 0x2080, v39
	s_waitcnt vmcnt(9)
	ds_write2_b32 v39, v0, v1 offset1:1
	ds_write2_b32 v39, v2, v3 offset0:2 offset1:3
	s_waitcnt vmcnt(8)
	ds_write2_b32 v40, v4, v5 offset1:1
	v_add_u32_e32 v40, 0x2088, v39
	ds_write2_b32 v40, v6, v7 offset1:1
	v_add_u32_e32 v40, 0x4100, v39
	s_waitcnt vmcnt(7)
	ds_write2_b32 v40, v8, v9 offset1:1
	v_add_u32_e32 v40, 0x4108, v39
	ds_write2_b32 v40, v10, v11 offset1:1
	v_add_u32_e32 v40, 0x6180, v39
	s_waitcnt vmcnt(6)
	ds_write2_b32 v40, v12, v13 offset1:1
	v_add_u32_e32 v40, 0x6188, v39
	ds_write2_b32 v40, v14, v15 offset1:1
	v_add_u32_e32 v40, 0x8200, v39
	s_waitcnt vmcnt(5)
	ds_write2_b32 v40, v16, v17 offset1:1
	v_add_u32_e32 v40, 0x8208, v39
	ds_write2_b32 v40, v18, v19 offset1:1
	v_add_u32_e32 v40, 0xa280, v39
	s_waitcnt vmcnt(4)
	ds_write2_b32 v40, v20, v21 offset1:1
	v_add_u32_e32 v40, 0xa288, v39
	ds_write2_b32 v40, v22, v23 offset1:1
	v_add_u32_e32 v40, 0xc300, v39
	s_waitcnt vmcnt(3)
	ds_write2_b32 v40, v24, v25 offset1:1
	v_add_u32_e32 v40, 0xc308, v39
	s_add_i32 s26, s28, s46
	ds_write2_b32 v40, v26, v27 offset1:1
	v_add_u32_e32 v40, 0xe380, v39
	s_cmpk_gt_i32 s26, 0xfff
	s_waitcnt vmcnt(2)
	ds_write2_b32 v40, v28, v29 offset1:1
	v_add_u32_e32 v40, 0xe388, v39
	s_cselect_b64 s[8:9], -1, 0
	s_cmpk_lt_i32 s26, 0x1000
	s_mov_b64 s[10:11], -1
	ds_write2_b32 v40, v30, v31 offset1:1
	s_waitcnt lgkmcnt(0)
	s_barrier
	s_cbranch_scc1 .LBB0_48
	s_add_i32 s27, s3, s2
	s_mov_b64 s[10:11], 0
